# speedup vs baseline: 1.0116x; 1.0116x over previous
.LBB2_64:
	v_bfe_u32 v34, v121, 16, 4
	v_cmp_gt_i32_e64 s[56:57], s66, v110
	v_lshl_add_u32 v115, v34, 1, v191
	v_lshlrev_b32_e32 v34, 2, v34
	ds_bpermute_b32 v121, v34, v197
	s_cmp_lt_i32 s66, 33
	s_cbranch_scc1 .Lmk_half_iter
	ds_read_b128 v[208:211], v122
	ds_read_b128 v[212:215], v117
	ds_read_b128 v[216:219], v122 offset:2048
	ds_read_b128 v[220:223], v117 offset:2048
	ds_read_b128 v[224:227], v122 offset:4096
	ds_read_b128 v[228:231], v117 offset:4096
	ds_read_b128 v[232:235], v122 offset:6144
	ds_read_b128 v[236:239], v117 offset:6144
	ds_read_b64_tr_b16 v[130:131], v186 offset:0
	ds_read_b64_tr_b16 v[132:133], v186 offset:2048
	ds_read_b64_tr_b16 v[134:135], v188 offset:0
	ds_read_b64_tr_b16 v[136:137], v188 offset:2048
	ds_read_b64_tr_b16 v[138:139], v189 offset:0
	ds_read_b64_tr_b16 v[140:141], v189 offset:2048
	ds_read_b64_tr_b16 v[142:143], v190 offset:0
	ds_read_b64_tr_b16 v[144:145], v190 offset:2048

.Lmk_half_join:
	v_cndmask_b32_e64 v34, v200, v160, s[60:61]
	v_cndmask_b32_e64 v34, v34, v248, s[62:63]
	v_cndmask_b32_e64 v34, v34, v252, s[64:65]
	v_cndmask_b32_e64 v201, v195, v185, s[54:55]
	v_add_f32_e32 v202, 0x40200000, v201
	v_add_f32_e32 v34, v34, v121
	v_mul_f32_e32 v121, 0x3e4ccccd, v34
	v_max_f32_e32 v34, v34, v121
	v_cmp_gt_f32_e32 vcc, v34, v202
	s_and_b64 s[68:69], s[56:57], vcc
	s_cmp_eq_u64 s[68:69], 0
	s_cbranch_scc0 .Lmk_max
	v_add_u32_e32 v229, s82, v172
	v_add_u32_e32 v230, s82, v173
	ds_read_u16 v224, v229 offset:0
	ds_read_u16 v225, v229 offset:32
	ds_read_u16 v226, v229 offset:64
	ds_read_u16 v227, v229 offset:96
	ds_read_u16 v232, v229 offset:128
	ds_read_u16 v233, v229 offset:160
	ds_read_u16 v234, v229 offset:192
	ds_read_u16 v235, v229 offset:224
	v_mov_b32_e32 v121, v183
	ds_read_b32 v183, v230

.Lmk_half_iter:
	ds_read_b128 v[208:211], v122
	ds_read_b128 v[212:215], v117
	ds_read_b128 v[216:219], v122 offset:2048
	ds_read_b128 v[220:223], v117 offset:2048
	ds_read_b64_tr_b16 v[130:131], v186 offset:0
	ds_read_b64_tr_b16 v[132:133], v186 offset:2048
	ds_read_b64_tr_b16 v[134:135], v188 offset:0
	ds_read_b64_tr_b16 v[136:137], v188 offset:2048
	ds_read_b64_tr_b16 v[138:139], v189 offset:0
	ds_read_b64_tr_b16 v[140:141], v189 offset:2048
	ds_read_b64_tr_b16 v[142:143], v190 offset:0
	ds_read_b64_tr_b16 v[144:145], v190 offset:2048
	s_waitcnt lgkmcnt(8)
	v_mfma_f32_16x16x32_f16 v[200:203], v[240:243], v[208:211], 0
	v_mfma_f32_16x16x32_f16 v[160:163], v[240:243], v[216:219], 0
	v_mfma_f32_16x16x32_f16 v[200:203], v[244:247], v[212:215], v[200:203]
	v_mfma_f32_16x16x32_f16 v[160:163], v[244:247], v[220:223], v[160:163]
	s_nop 6
	s_branch .Lmk_half_join
